# inproj0: 2-D XCD tile dealing (an XCD owns one M parity and 6 of the 24 N-tiles)
# speedup vs baseline: 1.0062x; 1.0037x over previous
; __device__ __forceinline__ void phase_inproj0(const Params& P, bfr* smem, int bid, int nb) {
;     ...
;     constexpr int nu = 65 * 24;
;     GemmPipe<256, 128, 1024, ALoadRows, BLoadT> gp;
;     ALoadRows al; BLoadT bl;
;     int u = bid;
;     if (u < nu) { al.init<256>(A, 1024, (u / 24) * 256, NT - 1, nullptr); bl.init<128>(Bt, 1024, (u % 24) * 128); gp.prefetch(al, bl); }
.LBB0_411:
	s_cmp_lt_i32 s6, 3
	s_cselect_b64 s[0:1], -1, 0
	s_cmp_gt_i32 s7, 2
	s_cselect_b64 s[2:3], -1, 0
	s_and_b64 s[0:1], s[0:1], s[2:3]
	s_andn2_b64 vcc, exec, s[0:1]
	s_cbranch_vccnz .LBB0_481
	v_readlane_b32 s97, v253, 10
	s_cmpk_lg_u32 s97, 0x100
	s_mov_b32 s97, s44
	s_cbranch_scc1 .Lip2_i
	s_lshr_b32 s96, s44, 3
	s_mul_i32 s97, s96, 10923
	s_lshr_b32 s97, s97, 16
	s_mul_i32 s97, s97, 42
	s_add_i32 s97, s97, s96
	s_and_b32 s98, s44, 1
	s_mul_i32 s98, s98, 24
	s_add_i32 s97, s97, s98
	s_bfe_u32 s98, s44, 0x20001
	s_mul_i32 s98, s98, 6
	s_add_i32 s97, s97, s98

; #define G_LOAD(SA, SB, KT) do { SA.load(al, (KT) * 32); SB.load(bl, (KT) * 32); } while (0)
; #define G_STORE(SA, SB, BUF) do { SA.store(As + (BUF) * ASZ, tid); SB.store(Bs3 + (BUF) * BSZ, tid); } while (0)
;     __device__ __forceinline__ void mainloop(bfr* smem, const AL& al, const BL& bl) {
;     ...
;         __syncthreads();
;         G_STORE(sa0, sb0, 0);
;         if (1 < nk) G_STORE(sa1, sb1, 1);
;         if (BL::DEPTH < nk) G_LOAD(sa0, sb0, BL::DEPTH);
;         if (BL::DEPTH + 1 < nk) G_LOAD(sa1, sb1, BL::DEPTH + 1);
;         __builtin_amdgcn_sched_barrier(0);
;         __syncthreads();
;         G_RD(fa0, fb0, 0);
;         if constexpr (BL::DEPTH == 3) {
; #pragma unroll
;             for (int kt = 0; kt < nk; kt += 6) {
;                 G_STEP(0, fa0, fb0, fa1, fb1, 1, sa2, sb2, 2, 3);
;                 G_STEP(1, fa1, fb1, fa0, fb0, 2, sa0, sb0, 0, 3);
;                 G_STEP(2, fa0, fb0, fa1, fb1, 0, sa1, sb1, 1, 3);
;                 G_STEP(3, fa1, fb1, fa0, fb0, 1, sa2, sb2, 2, 3);
;                 G_STEP(4, fa0, fb0, fa1, fb1, 2, sa0, sb0, 0, 3);
;                 G_STEP(5, fa1, fb1, fa0, fb0, 0, sa1, sb1, 1, 3);
.LBB0_415:
	s_barrier
	global_load_dwordx4 v[102:105], v[114:115], off offset:192
	global_load_dwordx4 v[106:109], v[114:115], off offset:256
	global_load_dwordx4 v[154:157], v[116:117], off offset:192
	global_load_dwordx4 v[158:161], v[116:117], off offset:256
	global_load_dwordx4 v[162:165], v[118:119], off offset:192
	global_load_dwordx4 v[166:169], v[118:119], off offset:256
	s_waitcnt vmcnt(7)
	ds_write_b128 v128, v[86:89] offset:16
	ds_write_b128 v129, v[78:81] offset:16
	ds_write_b128 v128, v[82:85] offset:61456
	ds_write_b128 v128, v[98:101] offset:20496
	ds_write_b128 v129, v[90:93] offset:20496
	ds_write_b128 v130, v[94:97]
	s_waitcnt lgkmcnt(0)
	s_barrier
	ds_read_b128 v[2:5], v132 offset:16
	ds_read_b128 v[78:81], v132 offset:48
	ds_read_b128 v[6:9], v152 offset:61456
	ds_read_b128 v[10:13], v132 offset:2576
	ds_read_b128 v[82:85], v132 offset:2608
	ds_read_b128 v[86:89], v152 offset:61488
	ds_read_b128 v[14:17], v152 offset:64016
	ds_read_b128 v[90:93], v152 offset:64048
	s_waitcnt lgkmcnt(5)
	v_mfma_f32_32x32x16_bf16 v[50:65], v[2:5], v[6:9], 0
	ds_read_b128 v[94:97], v132 offset:20496
	ds_read_b128 v[98:101], v133
	s_waitcnt lgkmcnt(3)
	v_mfma_f32_32x32x16_bf16 v[34:49], v[2:5], v[14:17], 0
	ds_read_b128 v[170:173], v132 offset:23056
	ds_read_b128 v[174:177], v134
	v_mfma_f32_32x32x16_bf16 v[18:33], v[10:13], v[6:9], 0
	ds_read_b128 v[178:181], v132 offset:20528
	ds_read_b128 v[182:185], v135
	v_mfma_f32_32x32x16_bf16 v[2:17], v[10:13], v[14:17], 0
	ds_read_b128 v[186:189], v132 offset:23088
	ds_read_b128 v[190:193], v136
	v_mfma_f32_32x32x16_bf16 v[50:65], v[78:81], v[86:89], v[50:65]
	ds_write_b128 v128, v[66:69] offset:40976
	ds_write_b128 v129, v[74:77] offset:40976
	s_waitcnt lgkmcnt(10)
	v_mfma_f32_32x32x16_bf16 v[34:49], v[78:81], v[90:93], v[34:49]
	s_waitcnt vmcnt(6)
	ds_write_b128 v137, v[70:73]
	v_mfma_f32_32x32x16_bf16 v[18:33], v[82:85], v[86:89], v[18:33]
	global_load_dwordx4 v[66:69], v[114:115], off offset:320
	global_load_dwordx4 v[70:73], v[116:117], off offset:320
	global_load_dwordx4 v[74:77], v[118:119], off offset:320
	v_mfma_f32_32x32x16_bf16 v[2:17], v[82:85], v[90:93], v[2:17]
	s_waitcnt lgkmcnt(0)
	s_barrier
	v_mfma_f32_32x32x16_bf16 v[50:65], v[94:97], v[98:101], v[50:65]
	ds_read_b128 v[78:81], v132 offset:40976
	ds_read_b128 v[82:85], v138
	v_mfma_f32_32x32x16_bf16 v[34:49], v[94:97], v[174:177], v[34:49]
	ds_read_b128 v[86:89], v132 offset:43536
	ds_read_b128 v[90:93], v139
	v_mfma_f32_32x32x16_bf16 v[18:33], v[170:173], v[98:101], v[18:33]
	ds_read_b128 v[94:97], v132 offset:41008
	ds_read_b128 v[98:101], v140
	v_mfma_f32_32x32x16_bf16 v[2:17], v[170:173], v[174:177], v[2:17]
	ds_read_b128 v[170:173], v132 offset:43568
	ds_read_b128 v[174:177], v141
	v_mfma_f32_32x32x16_bf16 v[50:65], v[178:181], v[182:185], v[50:65]
	s_waitcnt vmcnt(8)
	ds_write_b128 v128, v[102:105] offset:16
	s_waitcnt vmcnt(6)
	ds_write_b128 v129, v[154:157] offset:16
	v_mfma_f32_32x32x16_bf16 v[34:49], v[178:181], v[190:193], v[34:49]
	s_waitcnt vmcnt(4)
	ds_write_b128 v128, v[162:165] offset:61456
	v_mfma_f32_32x32x16_bf16 v[18:33], v[186:189], v[182:185], v[18:33]
	global_load_dwordx4 v[102:105], v[114:115], off offset:384
	global_load_dwordx4 v[154:157], v[116:117], off offset:384
	global_load_dwordx4 v[162:165], v[118:119], off offset:384
	v_mfma_f32_32x32x16_bf16 v[2:17], v[186:189], v[190:193], v[2:17]
	s_waitcnt lgkmcnt(0)
	s_barrier
	v_mfma_f32_32x32x16_bf16 v[50:65], v[78:81], v[82:85], v[50:65]
	ds_read_b128 v[178:181], v132 offset:16
	ds_read_b128 v[182:185], v142 offset:61456
	v_mfma_f32_32x32x16_bf16 v[34:49], v[78:81], v[90:93], v[34:49]
	ds_read_b128 v[78:81], v132 offset:2576
	ds_read_b128 v[186:189], v142 offset:64016
	v_mfma_f32_32x32x16_bf16 v[18:33], v[86:89], v[82:85], v[18:33]
	ds_read_b128 v[82:85], v132 offset:48
	ds_read_b128 v[190:193], v142 offset:61488
	v_mfma_f32_32x32x16_bf16 v[2:17], v[86:89], v[90:93], v[2:17]
	ds_read_b128 v[86:89], v132 offset:2608
	ds_read_b128 v[90:93], v143 offset:64016
	v_mfma_f32_32x32x16_bf16 v[50:65], v[94:97], v[98:101], v[50:65]
	ds_write_b128 v128, v[106:109] offset:20496
	ds_write_b128 v129, v[158:161] offset:20496
	v_mfma_f32_32x32x16_bf16 v[34:49], v[94:97], v[174:177], v[34:49]
	s_waitcnt vmcnt(6)
	ds_write_b128 v130, v[166:169]
	v_mfma_f32_32x32x16_bf16 v[18:33], v[170:173], v[98:101], v[18:33]
	global_load_dwordx4 v[94:97], v[114:115], off offset:448
	global_load_dwordx4 v[98:101], v[116:117], off offset:448
	global_load_dwordx4 v[106:109], v[118:119], off offset:448
	v_mfma_f32_32x32x16_bf16 v[2:17], v[170:173], v[174:177], v[2:17]
	s_waitcnt lgkmcnt(0)
	s_barrier
	v_mfma_f32_32x32x16_bf16 v[50:65], v[178:181], v[182:185], v[50:65]
	ds_read_b128 v[158:161], v132 offset:20496
	ds_read_b128 v[166:169], v133
	v_mfma_f32_32x32x16_bf16 v[34:49], v[178:181], v[186:189], v[34:49]
	ds_read_b128 v[170:173], v132 offset:23056
	ds_read_b128 v[174:177], v134
	v_mfma_f32_32x32x16_bf16 v[18:33], v[78:81], v[182:185], v[18:33]
	ds_read_b128 v[178:181], v132 offset:20528
	ds_read_b128 v[182:185], v135
	v_mfma_f32_32x32x16_bf16 v[2:17], v[78:81], v[186:189], v[2:17]
	ds_read_b128 v[78:81], v132 offset:23088
	ds_read_b128 v[186:189], v136
	v_mfma_f32_32x32x16_bf16 v[50:65], v[82:85], v[190:193], v[50:65]
	s_waitcnt vmcnt(8)
	ds_write_b128 v128, v[66:69] offset:40976
	s_waitcnt vmcnt(7)
	ds_write_b128 v129, v[70:73] offset:40976
	v_mfma_f32_32x32x16_bf16 v[34:49], v[82:85], v[90:93], v[34:49]
	s_waitcnt vmcnt(6)
	ds_write_b128 v137, v[74:77]
	v_mfma_f32_32x32x16_bf16 v[18:33], v[86:89], v[190:193], v[18:33]
	global_load_dwordx4 v[66:69], v[114:115], off offset:512
	global_load_dwordx4 v[70:73], v[116:117], off offset:512
	global_load_dwordx4 v[74:77], v[118:119], off offset:512
	v_mfma_f32_32x32x16_bf16 v[2:17], v[86:89], v[90:93], v[2:17]
	s_waitcnt lgkmcnt(0)
	s_barrier
;     __device__ __forceinline__ void mainloop(bfr* smem, const AL& al, const BL& bl) {
;     ...
;         if constexpr (BL::DEPTH == 3) {
; #pragma unroll
;             for (int kt = 0; kt < nk; kt += 6) {
;                 G_STEP(0, fa0, fb0, fa1, fb1, 1, sa2, sb2, 2, 3);
;                 G_STEP(1, fa1, fb1, fa0, fb0, 2, sa0, sb0, 0, 3);
;                 G_STEP(2, fa0, fb0, fa1, fb1, 0, sa1, sb1, 1, 3);
;                 G_STEP(3, fa1, fb1, fa0, fb0, 1, sa2, sb2, 2, 3);
;                 G_STEP(4, fa0, fb0, fa1, fb1, 2, sa0, sb0, 0, 3);
;                 G_STEP(5, fa1, fb1, fa0, fb0, 0, sa1, sb1, 1, 3);
;             }
	v_mfma_f32_32x32x16_bf16 v[50:65], v[158:161], v[166:169], v[50:65]
	ds_read_b128 v[82:85], v132 offset:40976
	ds_read_b128 v[86:89], v138
	v_mfma_f32_32x32x16_bf16 v[34:49], v[158:161], v[174:177], v[34:49]
	ds_read_b128 v[90:93], v132 offset:43536
	ds_read_b128 v[158:161], v139
	v_mfma_f32_32x32x16_bf16 v[18:33], v[170:173], v[166:169], v[18:33]
	ds_read_b128 v[166:169], v132 offset:41008
	ds_read_b128 v[190:193], v140
	v_mfma_f32_32x32x16_bf16 v[2:17], v[170:173], v[174:177], v[2:17]
	ds_read_b128 v[170:173], v132 offset:43568
	ds_read_b128 v[174:177], v141
	v_mfma_f32_32x32x16_bf16 v[50:65], v[178:181], v[182:185], v[50:65]
	s_waitcnt vmcnt(8)
	ds_write_b128 v128, v[102:105] offset:16
	s_waitcnt vmcnt(7)
	ds_write_b128 v129, v[154:157] offset:16
	v_mfma_f32_32x32x16_bf16 v[34:49], v[178:181], v[186:189], v[34:49]
	s_waitcnt vmcnt(6)
	ds_write_b128 v128, v[162:165] offset:61456
	v_mfma_f32_32x32x16_bf16 v[18:33], v[78:81], v[182:185], v[18:33]
	global_load_dwordx4 v[102:105], v[114:115], off offset:576
	global_load_dwordx4 v[154:157], v[116:117], off offset:576
	global_load_dwordx4 v[162:165], v[118:119], off offset:576
	v_mfma_f32_32x32x16_bf16 v[2:17], v[78:81], v[186:189], v[2:17]
	s_waitcnt lgkmcnt(0)
	s_barrier
	v_mfma_f32_32x32x16_bf16 v[50:65], v[82:85], v[86:89], v[50:65]
	ds_read_b128 v[78:81], v132 offset:16
	ds_read_b128 v[178:181], v142 offset:61456
	v_mfma_f32_32x32x16_bf16 v[34:49], v[82:85], v[158:161], v[34:49]
	ds_read_b128 v[82:85], v132 offset:2576
	ds_read_b128 v[182:185], v142 offset:64016
	v_mfma_f32_32x32x16_bf16 v[18:33], v[90:93], v[86:89], v[18:33]
	ds_read_b128 v[86:89], v132 offset:48
	ds_read_b128 v[186:189], v142 offset:61488
	v_mfma_f32_32x32x16_bf16 v[2:17], v[90:93], v[158:161], v[2:17]
	ds_read_b128 v[90:93], v132 offset:2608
	ds_read_b128 v[158:161], v143 offset:64016
	v_mfma_f32_32x32x16_bf16 v[50:65], v[166:169], v[190:193], v[50:65]
	s_waitcnt vmcnt(8)
	ds_write_b128 v128, v[94:97] offset:20496
	s_waitcnt vmcnt(7)
	ds_write_b128 v129, v[98:101] offset:20496
	v_mfma_f32_32x32x16_bf16 v[34:49], v[166:169], v[174:177], v[34:49]
	s_waitcnt vmcnt(6)
	ds_write_b128 v130, v[106:109]
	v_mfma_f32_32x32x16_bf16 v[18:33], v[170:173], v[190:193], v[18:33]
	global_load_dwordx4 v[94:97], v[114:115], off offset:640
	global_load_dwordx4 v[98:101], v[116:117], off offset:640
	global_load_dwordx4 v[106:109], v[118:119], off offset:640
	v_mfma_f32_32x32x16_bf16 v[2:17], v[170:173], v[174:177], v[2:17]
	s_waitcnt lgkmcnt(0)
	s_barrier
	v_mfma_f32_32x32x16_bf16 v[50:65], v[78:81], v[178:181], v[50:65]
	ds_read_b128 v[166:169], v132 offset:20496
	ds_read_b128 v[170:173], v133
	v_mfma_f32_32x32x16_bf16 v[34:49], v[78:81], v[182:185], v[34:49]
	ds_read_b128 v[78:81], v132 offset:23056
	ds_read_b128 v[174:177], v134
	v_mfma_f32_32x32x16_bf16 v[18:33], v[82:85], v[178:181], v[18:33]
	ds_read_b128 v[178:181], v132 offset:20528
	ds_read_b128 v[190:193], v135
	v_mfma_f32_32x32x16_bf16 v[2:17], v[82:85], v[182:185], v[2:17]
	ds_read_b128 v[82:85], v132 offset:23088
	ds_read_b128 v[182:185], v136
	v_mfma_f32_32x32x16_bf16 v[50:65], v[86:89], v[186:189], v[50:65]
	s_waitcnt vmcnt(8)
	ds_write_b128 v128, v[66:69] offset:40976
	s_waitcnt vmcnt(7)
	ds_write_b128 v129, v[70:73] offset:40976
	v_mfma_f32_32x32x16_bf16 v[34:49], v[86:89], v[158:161], v[34:49]
	s_waitcnt vmcnt(6)
	ds_write_b128 v137, v[74:77]
	v_mfma_f32_32x32x16_bf16 v[18:33], v[90:93], v[186:189], v[18:33]
	global_load_dwordx4 v[66:69], v[114:115], off offset:704
	global_load_dwordx4 v[70:73], v[116:117], off offset:704
	global_load_dwordx4 v[74:77], v[118:119], off offset:704
	v_mfma_f32_32x32x16_bf16 v[2:17], v[90:93], v[158:161], v[2:17]
	s_waitcnt lgkmcnt(0)
	s_barrier
	v_mfma_f32_32x32x16_bf16 v[50:65], v[166:169], v[170:173], v[50:65]
	ds_read_b128 v[86:89], v132 offset:40976
	ds_read_b128 v[90:93], v138
	v_mfma_f32_32x32x16_bf16 v[34:49], v[166:169], v[174:177], v[34:49]
	ds_read_b128 v[158:161], v132 offset:43536
	ds_read_b128 v[166:169], v139
	v_mfma_f32_32x32x16_bf16 v[18:33], v[78:81], v[170:173], v[18:33]
	ds_read_b128 v[170:173], v132 offset:41008
	ds_read_b128 v[186:189], v140
	v_mfma_f32_32x32x16_bf16 v[2:17], v[78:81], v[174:177], v[2:17]
	ds_read_b128 v[78:81], v132 offset:43568
	ds_read_b128 v[174:177], v141
	v_mfma_f32_32x32x16_bf16 v[50:65], v[178:181], v[190:193], v[50:65]
	s_waitcnt vmcnt(8)
	ds_write_b128 v128, v[102:105] offset:16
	s_waitcnt vmcnt(7)
	ds_write_b128 v129, v[154:157] offset:16
	v_mfma_f32_32x32x16_bf16 v[34:49], v[178:181], v[182:185], v[34:49]
	s_waitcnt vmcnt(6)
	ds_write_b128 v128, v[162:165] offset:61456
	v_mfma_f32_32x32x16_bf16 v[18:33], v[82:85], v[190:193], v[18:33]
	global_load_dwordx4 v[102:105], v[114:115], off offset:768
	global_load_dwordx4 v[154:157], v[116:117], off offset:768
	global_load_dwordx4 v[162:165], v[118:119], off offset:768
	v_mfma_f32_32x32x16_bf16 v[2:17], v[82:85], v[182:185], v[2:17]
	s_waitcnt lgkmcnt(0)
	s_barrier
	v_mfma_f32_32x32x16_bf16 v[50:65], v[86:89], v[90:93], v[50:65]
	ds_read_b128 v[82:85], v132 offset:16
	ds_read_b128 v[178:181], v142 offset:61456
	v_mfma_f32_32x32x16_bf16 v[34:49], v[86:89], v[166:169], v[34:49]
	ds_read_b128 v[86:89], v132 offset:2576
	ds_read_b128 v[182:185], v142 offset:64016
	v_mfma_f32_32x32x16_bf16 v[18:33], v[158:161], v[90:93], v[18:33]
	ds_read_b128 v[90:93], v132 offset:48
	ds_read_b128 v[190:193], v142 offset:61488
	v_mfma_f32_32x32x16_bf16 v[2:17], v[158:161], v[166:169], v[2:17]
	ds_read_b128 v[158:161], v132 offset:2608
	ds_read_b128 v[166:169], v143 offset:64016
	v_mfma_f32_32x32x16_bf16 v[50:65], v[170:173], v[186:189], v[50:65]
	s_waitcnt vmcnt(8)
	ds_write_b128 v128, v[94:97] offset:20496
	s_waitcnt vmcnt(7)
	ds_write_b128 v129, v[98:101] offset:20496
	v_mfma_f32_32x32x16_bf16 v[34:49], v[170:173], v[174:177], v[34:49]
	s_waitcnt vmcnt(6)
	ds_write_b128 v130, v[106:109]
	v_mfma_f32_32x32x16_bf16 v[18:33], v[78:81], v[186:189], v[18:33]
	global_load_dwordx4 v[94:97], v[114:115], off offset:832
	global_load_dwordx4 v[98:101], v[116:117], off offset:832
	global_load_dwordx4 v[106:109], v[118:119], off offset:832
	v_mfma_f32_32x32x16_bf16 v[2:17], v[78:81], v[174:177], v[2:17]
	s_waitcnt lgkmcnt(0)
	s_barrier
;     __device__ __forceinline__ void mainloop(bfr* smem, const AL& al, const BL& bl) {
;     ...
;         if constexpr (BL::DEPTH == 3) {
; #pragma unroll
;             for (int kt = 0; kt < nk; kt += 6) {
;                 G_STEP(0, fa0, fb0, fa1, fb1, 1, sa2, sb2, 2, 3);
;                 G_STEP(1, fa1, fb1, fa0, fb0, 2, sa0, sb0, 0, 3);
;                 G_STEP(2, fa0, fb0, fa1, fb1, 0, sa1, sb1, 1, 3);
;                 G_STEP(3, fa1, fb1, fa0, fb0, 1, sa2, sb2, 2, 3);
;                 G_STEP(4, fa0, fb0, fa1, fb1, 2, sa0, sb0, 0, 3);
;                 G_STEP(5, fa1, fb1, fa0, fb0, 0, sa1, sb1, 1, 3);
;             }
	v_mfma_f32_32x32x16_bf16 v[50:65], v[82:85], v[178:181], v[50:65]
	ds_read_b128 v[78:81], v132 offset:20496
	ds_read_b128 v[170:173], v133
	v_mfma_f32_32x32x16_bf16 v[34:49], v[82:85], v[182:185], v[34:49]
	ds_read_b128 v[82:85], v132 offset:23056
	ds_read_b128 v[174:177], v134
	v_mfma_f32_32x32x16_bf16 v[18:33], v[86:89], v[178:181], v[18:33]
	ds_read_b128 v[178:181], v132 offset:20528
	ds_read_b128 v[186:189], v135
	v_mfma_f32_32x32x16_bf16 v[2:17], v[86:89], v[182:185], v[2:17]
	ds_read_b128 v[86:89], v132 offset:23088
	ds_read_b128 v[182:185], v136
	v_mfma_f32_32x32x16_bf16 v[50:65], v[90:93], v[190:193], v[50:65]
	s_waitcnt vmcnt(8)
	ds_write_b128 v128, v[66:69] offset:40976
	s_waitcnt vmcnt(7)
	ds_write_b128 v129, v[70:73] offset:40976
	v_mfma_f32_32x32x16_bf16 v[34:49], v[90:93], v[166:169], v[34:49]
	s_waitcnt vmcnt(6)
	ds_write_b128 v137, v[74:77]
	v_mfma_f32_32x32x16_bf16 v[18:33], v[158:161], v[190:193], v[18:33]
	global_load_dwordx4 v[66:69], v[114:115], off offset:896
	global_load_dwordx4 v[70:73], v[116:117], off offset:896
	global_load_dwordx4 v[74:77], v[118:119], off offset:896
	v_mfma_f32_32x32x16_bf16 v[2:17], v[158:161], v[166:169], v[2:17]
	s_waitcnt lgkmcnt(0)
	s_barrier
	v_mfma_f32_32x32x16_bf16 v[50:65], v[78:81], v[170:173], v[50:65]
	ds_read_b128 v[90:93], v132 offset:40976
	ds_read_b128 v[158:161], v138
	v_mfma_f32_32x32x16_bf16 v[34:49], v[78:81], v[174:177], v[34:49]
	ds_read_b128 v[78:81], v132 offset:43536
	ds_read_b128 v[166:169], v139
	v_mfma_f32_32x32x16_bf16 v[18:33], v[82:85], v[170:173], v[18:33]
	ds_read_b128 v[170:173], v132 offset:41008
	ds_read_b128 v[190:193], v140
	v_mfma_f32_32x32x16_bf16 v[2:17], v[82:85], v[174:177], v[2:17]
	ds_read_b128 v[82:85], v132 offset:43568
	ds_read_b128 v[174:177], v141
	v_mfma_f32_32x32x16_bf16 v[50:65], v[178:181], v[186:189], v[50:65]
	s_waitcnt vmcnt(8)
	ds_write_b128 v128, v[102:105] offset:16
	s_waitcnt vmcnt(7)
	ds_write_b128 v129, v[154:157] offset:16
	v_mfma_f32_32x32x16_bf16 v[34:49], v[178:181], v[182:185], v[34:49]
	s_waitcnt vmcnt(6)
	ds_write_b128 v128, v[162:165] offset:61456
	v_mfma_f32_32x32x16_bf16 v[18:33], v[86:89], v[186:189], v[18:33]
	global_load_dwordx4 v[102:105], v[114:115], off offset:960
	global_load_dwordx4 v[154:157], v[116:117], off offset:960
	global_load_dwordx4 v[162:165], v[118:119], off offset:960
	v_mfma_f32_32x32x16_bf16 v[2:17], v[86:89], v[182:185], v[2:17]
	s_waitcnt lgkmcnt(0)
	s_barrier
	v_mfma_f32_32x32x16_bf16 v[50:65], v[90:93], v[158:161], v[50:65]
	ds_read_b128 v[86:89], v132 offset:16
	ds_read_b128 v[178:181], v142 offset:61456
	v_mfma_f32_32x32x16_bf16 v[34:49], v[90:93], v[166:169], v[34:49]
	ds_read_b128 v[90:93], v132 offset:2576
	ds_read_b128 v[182:185], v142 offset:64016
	v_mfma_f32_32x32x16_bf16 v[18:33], v[78:81], v[158:161], v[18:33]
	ds_read_b128 v[158:161], v132 offset:48
	ds_read_b128 v[186:189], v142 offset:61488
	v_mfma_f32_32x32x16_bf16 v[2:17], v[78:81], v[166:169], v[2:17]
	ds_read_b128 v[78:81], v132 offset:2608
	ds_read_b128 v[166:169], v143 offset:64016
	v_mfma_f32_32x32x16_bf16 v[50:65], v[170:173], v[190:193], v[50:65]
	s_waitcnt vmcnt(8)
	ds_write_b128 v128, v[94:97] offset:20496
	s_waitcnt vmcnt(7)
	ds_write_b128 v129, v[98:101] offset:20496
	v_mfma_f32_32x32x16_bf16 v[34:49], v[170:173], v[174:177], v[34:49]
	s_waitcnt vmcnt(6)
	ds_write_b128 v130, v[106:109]
	v_mfma_f32_32x32x16_bf16 v[18:33], v[82:85], v[190:193], v[18:33]
	global_load_dwordx4 v[94:97], v[114:115], off offset:1024
	global_load_dwordx4 v[98:101], v[116:117], off offset:1024
	global_load_dwordx4 v[106:109], v[118:119], off offset:1024
	v_mfma_f32_32x32x16_bf16 v[2:17], v[82:85], v[174:177], v[2:17]
	s_waitcnt lgkmcnt(0)
	s_barrier
	v_mfma_f32_32x32x16_bf16 v[50:65], v[86:89], v[178:181], v[50:65]
	ds_read_b128 v[82:85], v132 offset:20496
	ds_read_b128 v[170:173], v133
	v_mfma_f32_32x32x16_bf16 v[34:49], v[86:89], v[182:185], v[34:49]
	ds_read_b128 v[86:89], v132 offset:23056
	ds_read_b128 v[174:177], v134
	v_mfma_f32_32x32x16_bf16 v[18:33], v[90:93], v[178:181], v[18:33]
	ds_read_b128 v[178:181], v132 offset:20528
	ds_read_b128 v[190:193], v135
	v_mfma_f32_32x32x16_bf16 v[2:17], v[90:93], v[182:185], v[2:17]
	ds_read_b128 v[90:93], v132 offset:23088
	ds_read_b128 v[182:185], v136
	v_mfma_f32_32x32x16_bf16 v[50:65], v[158:161], v[186:189], v[50:65]
	s_waitcnt vmcnt(8)
	ds_write_b128 v128, v[66:69] offset:40976
	s_waitcnt vmcnt(7)
	ds_write_b128 v129, v[70:73] offset:40976
	v_mfma_f32_32x32x16_bf16 v[34:49], v[158:161], v[166:169], v[34:49]
	s_waitcnt vmcnt(6)
	ds_write_b128 v137, v[74:77]
	v_mfma_f32_32x32x16_bf16 v[18:33], v[78:81], v[186:189], v[18:33]
	global_load_dwordx4 v[66:69], v[114:115], off offset:1088
	global_load_dwordx4 v[70:73], v[116:117], off offset:1088
	global_load_dwordx4 v[74:77], v[118:119], off offset:1088
	v_mfma_f32_32x32x16_bf16 v[2:17], v[78:81], v[166:169], v[2:17]
	s_waitcnt lgkmcnt(0)
	s_barrier
	v_mfma_f32_32x32x16_bf16 v[50:65], v[82:85], v[170:173], v[50:65]
	ds_read_b128 v[78:81], v132 offset:40976
	ds_read_b128 v[158:161], v138
	v_mfma_f32_32x32x16_bf16 v[34:49], v[82:85], v[174:177], v[34:49]
	ds_read_b128 v[82:85], v132 offset:43536
	ds_read_b128 v[166:169], v139
	v_mfma_f32_32x32x16_bf16 v[18:33], v[86:89], v[170:173], v[18:33]
	ds_read_b128 v[170:173], v132 offset:41008
	ds_read_b128 v[186:189], v140
	v_mfma_f32_32x32x16_bf16 v[2:17], v[86:89], v[174:177], v[2:17]
	ds_read_b128 v[86:89], v132 offset:43568
	ds_read_b128 v[174:177], v141
	v_mfma_f32_32x32x16_bf16 v[50:65], v[178:181], v[190:193], v[50:65]
	s_waitcnt vmcnt(8)
	ds_write_b128 v128, v[102:105] offset:16
	s_waitcnt vmcnt(7)
	ds_write_b128 v129, v[154:157] offset:16
	v_mfma_f32_32x32x16_bf16 v[34:49], v[178:181], v[182:185], v[34:49]
	s_waitcnt vmcnt(6)
	ds_write_b128 v128, v[162:165] offset:61456
	v_mfma_f32_32x32x16_bf16 v[18:33], v[90:93], v[190:193], v[18:33]
	global_load_dwordx4 v[102:105], v[114:115], off offset:1152
	global_load_dwordx4 v[154:157], v[116:117], off offset:1152
	global_load_dwordx4 v[162:165], v[118:119], off offset:1152
	v_mfma_f32_32x32x16_bf16 v[2:17], v[90:93], v[182:185], v[2:17]
	s_waitcnt lgkmcnt(0)
	s_barrier
;     __device__ __forceinline__ void mainloop(bfr* smem, const AL& al, const BL& bl) {
;     ...
;         if constexpr (BL::DEPTH == 3) {
; #pragma unroll
;             for (int kt = 0; kt < nk; kt += 6) {
;                 G_STEP(0, fa0, fb0, fa1, fb1, 1, sa2, sb2, 2, 3);
;                 G_STEP(1, fa1, fb1, fa0, fb0, 2, sa0, sb0, 0, 3);
;                 G_STEP(2, fa0, fb0, fa1, fb1, 0, sa1, sb1, 1, 3);
;                 G_STEP(3, fa1, fb1, fa0, fb0, 1, sa2, sb2, 2, 3);
;                 G_STEP(4, fa0, fb0, fa1, fb1, 2, sa0, sb0, 0, 3);
;                 G_STEP(5, fa1, fb1, fa0, fb0, 0, sa1, sb1, 1, 3);
;             }
	v_mfma_f32_32x32x16_bf16 v[50:65], v[78:81], v[158:161], v[50:65]
	ds_read_b128 v[90:93], v132 offset:16
	ds_read_b128 v[178:181], v142 offset:61456
	v_mfma_f32_32x32x16_bf16 v[34:49], v[78:81], v[166:169], v[34:49]
	ds_read_b128 v[78:81], v132 offset:2576
	ds_read_b128 v[182:185], v142 offset:64016
	v_mfma_f32_32x32x16_bf16 v[18:33], v[82:85], v[158:161], v[18:33]
	ds_read_b128 v[158:161], v132 offset:48
	ds_read_b128 v[190:193], v142 offset:61488
	v_mfma_f32_32x32x16_bf16 v[2:17], v[82:85], v[166:169], v[2:17]
	ds_read_b128 v[82:85], v132 offset:2608
	ds_read_b128 v[166:169], v143 offset:64016
	v_mfma_f32_32x32x16_bf16 v[50:65], v[170:173], v[186:189], v[50:65]
	s_waitcnt vmcnt(8)
	ds_write_b128 v128, v[94:97] offset:20496
	s_waitcnt vmcnt(7)
	ds_write_b128 v129, v[98:101] offset:20496
	v_mfma_f32_32x32x16_bf16 v[34:49], v[170:173], v[174:177], v[34:49]
	s_waitcnt vmcnt(6)
	ds_write_b128 v130, v[106:109]
	v_mfma_f32_32x32x16_bf16 v[18:33], v[86:89], v[186:189], v[18:33]
	global_load_dwordx4 v[94:97], v[114:115], off offset:1216
	global_load_dwordx4 v[98:101], v[116:117], off offset:1216
	global_load_dwordx4 v[106:109], v[118:119], off offset:1216
	v_mfma_f32_32x32x16_bf16 v[2:17], v[86:89], v[174:177], v[2:17]
	s_waitcnt lgkmcnt(0)
	s_barrier
	v_mfma_f32_32x32x16_bf16 v[50:65], v[90:93], v[178:181], v[50:65]
	ds_read_b128 v[86:89], v132 offset:20496
	ds_read_b128 v[170:173], v133
	v_mfma_f32_32x32x16_bf16 v[34:49], v[90:93], v[182:185], v[34:49]
	ds_read_b128 v[90:93], v132 offset:23056
	ds_read_b128 v[174:177], v134
	v_mfma_f32_32x32x16_bf16 v[18:33], v[78:81], v[178:181], v[18:33]
	ds_read_b128 v[178:181], v132 offset:20528
	ds_read_b128 v[186:189], v135
	v_mfma_f32_32x32x16_bf16 v[2:17], v[78:81], v[182:185], v[2:17]
	ds_read_b128 v[78:81], v132 offset:23088
	ds_read_b128 v[182:185], v136
	v_mfma_f32_32x32x16_bf16 v[50:65], v[158:161], v[190:193], v[50:65]
	s_waitcnt vmcnt(8)
	ds_write_b128 v128, v[66:69] offset:40976
	s_waitcnt vmcnt(7)
	ds_write_b128 v129, v[70:73] offset:40976
	v_mfma_f32_32x32x16_bf16 v[34:49], v[158:161], v[166:169], v[34:49]
	s_waitcnt vmcnt(6)
	ds_write_b128 v137, v[74:77]
	v_mfma_f32_32x32x16_bf16 v[18:33], v[82:85], v[190:193], v[18:33]
	global_load_dwordx4 v[66:69], v[114:115], off offset:1280
	global_load_dwordx4 v[70:73], v[116:117], off offset:1280
	global_load_dwordx4 v[74:77], v[118:119], off offset:1280
	v_mfma_f32_32x32x16_bf16 v[2:17], v[82:85], v[166:169], v[2:17]
	s_waitcnt lgkmcnt(0)
	s_barrier
	v_mfma_f32_32x32x16_bf16 v[50:65], v[86:89], v[170:173], v[50:65]
	ds_read_b128 v[82:85], v132 offset:40976
	ds_read_b128 v[158:161], v138
	v_mfma_f32_32x32x16_bf16 v[34:49], v[86:89], v[174:177], v[34:49]
	ds_read_b128 v[86:89], v132 offset:43536
	ds_read_b128 v[166:169], v139
	v_mfma_f32_32x32x16_bf16 v[18:33], v[90:93], v[170:173], v[18:33]
	ds_read_b128 v[170:173], v132 offset:41008
	ds_read_b128 v[190:193], v140
	v_mfma_f32_32x32x16_bf16 v[2:17], v[90:93], v[174:177], v[2:17]
	ds_read_b128 v[90:93], v132 offset:43568
	ds_read_b128 v[174:177], v141
	v_mfma_f32_32x32x16_bf16 v[50:65], v[178:181], v[186:189], v[50:65]
	s_waitcnt vmcnt(8)
	ds_write_b128 v128, v[102:105] offset:16
	s_waitcnt vmcnt(7)
	ds_write_b128 v129, v[154:157] offset:16
	v_mfma_f32_32x32x16_bf16 v[34:49], v[178:181], v[182:185], v[34:49]
	s_waitcnt vmcnt(6)
	ds_write_b128 v128, v[162:165] offset:61456
	v_mfma_f32_32x32x16_bf16 v[18:33], v[78:81], v[186:189], v[18:33]
	global_load_dwordx4 v[102:105], v[114:115], off offset:1344
	global_load_dwordx4 v[154:157], v[116:117], off offset:1344
	global_load_dwordx4 v[162:165], v[118:119], off offset:1344
	v_mfma_f32_32x32x16_bf16 v[2:17], v[78:81], v[182:185], v[2:17]
	s_waitcnt lgkmcnt(0)
	s_barrier
	v_mfma_f32_32x32x16_bf16 v[50:65], v[82:85], v[158:161], v[50:65]
	ds_read_b128 v[78:81], v132 offset:16
	ds_read_b128 v[178:181], v142 offset:61456
	v_mfma_f32_32x32x16_bf16 v[34:49], v[82:85], v[166:169], v[34:49]
	ds_read_b128 v[82:85], v132 offset:2576
	ds_read_b128 v[182:185], v142 offset:64016
	v_mfma_f32_32x32x16_bf16 v[18:33], v[86:89], v[158:161], v[18:33]
	ds_read_b128 v[158:161], v132 offset:48
	ds_read_b128 v[186:189], v142 offset:61488
	v_mfma_f32_32x32x16_bf16 v[2:17], v[86:89], v[166:169], v[2:17]
	ds_read_b128 v[86:89], v132 offset:2608
	ds_read_b128 v[166:169], v143 offset:64016
	v_mfma_f32_32x32x16_bf16 v[50:65], v[170:173], v[190:193], v[50:65]
	s_waitcnt vmcnt(8)
	ds_write_b128 v128, v[94:97] offset:20496
	s_waitcnt vmcnt(7)
	ds_write_b128 v129, v[98:101] offset:20496
	v_mfma_f32_32x32x16_bf16 v[34:49], v[170:173], v[174:177], v[34:49]
	s_waitcnt vmcnt(6)
	ds_write_b128 v130, v[106:109]
	v_mfma_f32_32x32x16_bf16 v[18:33], v[90:93], v[190:193], v[18:33]
	global_load_dwordx4 v[94:97], v[114:115], off offset:1408
	global_load_dwordx4 v[98:101], v[116:117], off offset:1408
	global_load_dwordx4 v[106:109], v[118:119], off offset:1408
	v_mfma_f32_32x32x16_bf16 v[2:17], v[90:93], v[174:177], v[2:17]
	s_waitcnt lgkmcnt(0)
	s_barrier
	v_mfma_f32_32x32x16_bf16 v[50:65], v[78:81], v[178:181], v[50:65]
	ds_read_b128 v[90:93], v132 offset:20496
	ds_read_b128 v[170:173], v133
	v_mfma_f32_32x32x16_bf16 v[34:49], v[78:81], v[182:185], v[34:49]
	ds_read_b128 v[78:81], v132 offset:23056
	ds_read_b128 v[174:177], v134
	v_mfma_f32_32x32x16_bf16 v[18:33], v[82:85], v[178:181], v[18:33]
	ds_read_b128 v[178:181], v132 offset:20528
	ds_read_b128 v[190:193], v135
	v_mfma_f32_32x32x16_bf16 v[2:17], v[82:85], v[182:185], v[2:17]
	ds_read_b128 v[82:85], v132 offset:23088
	ds_read_b128 v[182:185], v136
	v_mfma_f32_32x32x16_bf16 v[50:65], v[158:161], v[186:189], v[50:65]
	s_waitcnt vmcnt(8)
	ds_write_b128 v128, v[66:69] offset:40976
	s_waitcnt vmcnt(7)
	ds_write_b128 v129, v[70:73] offset:40976
	v_mfma_f32_32x32x16_bf16 v[34:49], v[158:161], v[166:169], v[34:49]
	s_waitcnt vmcnt(6)
	ds_write_b128 v137, v[74:77]
	v_mfma_f32_32x32x16_bf16 v[18:33], v[86:89], v[186:189], v[18:33]
	global_load_dwordx4 v[66:69], v[114:115], off offset:1472
	global_load_dwordx4 v[70:73], v[116:117], off offset:1472
	global_load_dwordx4 v[74:77], v[118:119], off offset:1472
	v_mfma_f32_32x32x16_bf16 v[2:17], v[86:89], v[166:169], v[2:17]
	s_waitcnt lgkmcnt(0)
	s_barrier
;     __device__ __forceinline__ void mainloop(bfr* smem, const AL& al, const BL& bl) {
;     ...
;         if constexpr (BL::DEPTH == 3) {
; #pragma unroll
;             for (int kt = 0; kt < nk; kt += 6) {
;                 G_STEP(0, fa0, fb0, fa1, fb1, 1, sa2, sb2, 2, 3);
;                 G_STEP(1, fa1, fb1, fa0, fb0, 2, sa0, sb0, 0, 3);
;                 G_STEP(2, fa0, fb0, fa1, fb1, 0, sa1, sb1, 1, 3);
;                 G_STEP(3, fa1, fb1, fa0, fb0, 1, sa2, sb2, 2, 3);
;                 G_STEP(4, fa0, fb0, fa1, fb1, 2, sa0, sb0, 0, 3);
;                 G_STEP(5, fa1, fb1, fa0, fb0, 0, sa1, sb1, 1, 3);
;             }
	v_mfma_f32_32x32x16_bf16 v[50:65], v[90:93], v[170:173], v[50:65]
	ds_read_b128 v[86:89], v132 offset:40976
	ds_read_b128 v[158:161], v138
	v_mfma_f32_32x32x16_bf16 v[34:49], v[90:93], v[174:177], v[34:49]
	ds_read_b128 v[90:93], v132 offset:43536
	ds_read_b128 v[166:169], v139
	v_mfma_f32_32x32x16_bf16 v[18:33], v[78:81], v[170:173], v[18:33]
	ds_read_b128 v[170:173], v132 offset:41008
	ds_read_b128 v[186:189], v140
	v_mfma_f32_32x32x16_bf16 v[2:17], v[78:81], v[174:177], v[2:17]
	ds_read_b128 v[78:81], v132 offset:43568
	ds_read_b128 v[174:177], v141
	v_mfma_f32_32x32x16_bf16 v[50:65], v[178:181], v[190:193], v[50:65]
	s_waitcnt vmcnt(8)
	ds_write_b128 v128, v[102:105] offset:16
	s_waitcnt vmcnt(7)
	ds_write_b128 v129, v[154:157] offset:16
	v_mfma_f32_32x32x16_bf16 v[34:49], v[178:181], v[182:185], v[34:49]
	s_waitcnt vmcnt(6)
	ds_write_b128 v128, v[162:165] offset:61456
	v_mfma_f32_32x32x16_bf16 v[18:33], v[82:85], v[190:193], v[18:33]
	global_load_dwordx4 v[102:105], v[114:115], off offset:1536
	global_load_dwordx4 v[154:157], v[116:117], off offset:1536
	global_load_dwordx4 v[162:165], v[118:119], off offset:1536
	v_mfma_f32_32x32x16_bf16 v[2:17], v[82:85], v[182:185], v[2:17]
	s_waitcnt lgkmcnt(0)
	s_barrier
	v_mfma_f32_32x32x16_bf16 v[50:65], v[86:89], v[158:161], v[50:65]
	ds_read_b128 v[82:85], v132 offset:16
	ds_read_b128 v[178:181], v142 offset:61456
	v_mfma_f32_32x32x16_bf16 v[34:49], v[86:89], v[166:169], v[34:49]
	ds_read_b128 v[86:89], v132 offset:2576
	ds_read_b128 v[182:185], v142 offset:64016
	v_mfma_f32_32x32x16_bf16 v[18:33], v[90:93], v[158:161], v[18:33]
	ds_read_b128 v[158:161], v132 offset:48
	ds_read_b128 v[190:193], v142 offset:61488
	v_mfma_f32_32x32x16_bf16 v[2:17], v[90:93], v[166:169], v[2:17]
	ds_read_b128 v[90:93], v132 offset:2608
	ds_read_b128 v[166:169], v143 offset:64016
	v_mfma_f32_32x32x16_bf16 v[50:65], v[170:173], v[186:189], v[50:65]
	s_waitcnt vmcnt(8)
	ds_write_b128 v128, v[94:97] offset:20496
	s_waitcnt vmcnt(7)
	ds_write_b128 v129, v[98:101] offset:20496
	v_mfma_f32_32x32x16_bf16 v[34:49], v[170:173], v[174:177], v[34:49]
	s_waitcnt vmcnt(6)
	ds_write_b128 v130, v[106:109]
	v_mfma_f32_32x32x16_bf16 v[18:33], v[78:81], v[186:189], v[18:33]
	global_load_dwordx4 v[94:97], v[114:115], off offset:1600
	global_load_dwordx4 v[98:101], v[116:117], off offset:1600
	global_load_dwordx4 v[106:109], v[118:119], off offset:1600
	v_mfma_f32_32x32x16_bf16 v[2:17], v[78:81], v[174:177], v[2:17]
	s_waitcnt lgkmcnt(0)
	s_barrier
	v_mfma_f32_32x32x16_bf16 v[50:65], v[82:85], v[178:181], v[50:65]
	ds_read_b128 v[78:81], v132 offset:20496
	ds_read_b128 v[170:173], v133
	v_mfma_f32_32x32x16_bf16 v[34:49], v[82:85], v[182:185], v[34:49]
	ds_read_b128 v[82:85], v132 offset:23056
	ds_read_b128 v[174:177], v134
	v_mfma_f32_32x32x16_bf16 v[18:33], v[86:89], v[178:181], v[18:33]
	ds_read_b128 v[178:181], v132 offset:20528
	ds_read_b128 v[186:189], v135
	v_mfma_f32_32x32x16_bf16 v[2:17], v[86:89], v[182:185], v[2:17]
	ds_read_b128 v[86:89], v132 offset:23088
	ds_read_b128 v[182:185], v136
	v_mfma_f32_32x32x16_bf16 v[50:65], v[158:161], v[190:193], v[50:65]
	s_waitcnt vmcnt(8)
	ds_write_b128 v128, v[66:69] offset:40976
	s_waitcnt vmcnt(7)
	ds_write_b128 v129, v[70:73] offset:40976
	v_mfma_f32_32x32x16_bf16 v[34:49], v[158:161], v[166:169], v[34:49]
	s_waitcnt vmcnt(6)
	ds_write_b128 v137, v[74:77]
	v_mfma_f32_32x32x16_bf16 v[18:33], v[90:93], v[190:193], v[18:33]
	global_load_dwordx4 v[66:69], v[114:115], off offset:1664
	global_load_dwordx4 v[70:73], v[116:117], off offset:1664
	global_load_dwordx4 v[74:77], v[118:119], off offset:1664
	v_mfma_f32_32x32x16_bf16 v[2:17], v[90:93], v[166:169], v[2:17]
	s_waitcnt lgkmcnt(0)
	s_barrier
	v_mfma_f32_32x32x16_bf16 v[50:65], v[78:81], v[170:173], v[50:65]
	ds_read_b128 v[90:93], v132 offset:40976
	ds_read_b128 v[158:161], v138
	v_mfma_f32_32x32x16_bf16 v[34:49], v[78:81], v[174:177], v[34:49]
	ds_read_b128 v[78:81], v132 offset:43536
	ds_read_b128 v[166:169], v139
	v_mfma_f32_32x32x16_bf16 v[18:33], v[82:85], v[170:173], v[18:33]
	ds_read_b128 v[170:173], v132 offset:41008
	ds_read_b128 v[190:193], v140
	v_mfma_f32_32x32x16_bf16 v[2:17], v[82:85], v[174:177], v[2:17]
	ds_read_b128 v[82:85], v132 offset:43568
	ds_read_b128 v[174:177], v141
	v_mfma_f32_32x32x16_bf16 v[50:65], v[178:181], v[186:189], v[50:65]
	s_waitcnt vmcnt(8)
	ds_write_b128 v128, v[102:105] offset:16
	s_waitcnt vmcnt(7)
	ds_write_b128 v129, v[154:157] offset:16
	v_mfma_f32_32x32x16_bf16 v[34:49], v[178:181], v[182:185], v[34:49]
	s_waitcnt vmcnt(6)
	ds_write_b128 v128, v[162:165] offset:61456
	v_mfma_f32_32x32x16_bf16 v[18:33], v[86:89], v[186:189], v[18:33]
	global_load_dwordx4 v[102:105], v[114:115], off offset:1728
	global_load_dwordx4 v[154:157], v[116:117], off offset:1728
	global_load_dwordx4 v[162:165], v[118:119], off offset:1728
	v_mfma_f32_32x32x16_bf16 v[2:17], v[86:89], v[182:185], v[2:17]
	s_waitcnt lgkmcnt(0)
	s_barrier
	v_mfma_f32_32x32x16_bf16 v[50:65], v[90:93], v[158:161], v[50:65]
	ds_read_b128 v[86:89], v132 offset:16
	ds_read_b128 v[178:181], v142 offset:61456
	v_mfma_f32_32x32x16_bf16 v[34:49], v[90:93], v[166:169], v[34:49]
	ds_read_b128 v[90:93], v132 offset:2576
	ds_read_b128 v[182:185], v142 offset:64016
	v_mfma_f32_32x32x16_bf16 v[18:33], v[78:81], v[158:161], v[18:33]
	ds_read_b128 v[158:161], v132 offset:48
	ds_read_b128 v[186:189], v142 offset:61488
	v_mfma_f32_32x32x16_bf16 v[2:17], v[78:81], v[166:169], v[2:17]
	ds_read_b128 v[78:81], v132 offset:2608
	ds_read_b128 v[166:169], v143 offset:64016
	v_mfma_f32_32x32x16_bf16 v[50:65], v[170:173], v[190:193], v[50:65]
	s_waitcnt vmcnt(8)
	ds_write_b128 v128, v[94:97] offset:20496
	s_waitcnt vmcnt(7)
	ds_write_b128 v129, v[98:101] offset:20496
	v_mfma_f32_32x32x16_bf16 v[34:49], v[170:173], v[174:177], v[34:49]
	s_waitcnt vmcnt(6)
	ds_write_b128 v130, v[106:109]
	v_mfma_f32_32x32x16_bf16 v[18:33], v[82:85], v[190:193], v[18:33]
	global_load_dwordx4 v[94:97], v[114:115], off offset:1792
	global_load_dwordx4 v[98:101], v[116:117], off offset:1792
	global_load_dwordx4 v[106:109], v[118:119], off offset:1792
	v_mfma_f32_32x32x16_bf16 v[2:17], v[82:85], v[174:177], v[2:17]
	s_waitcnt lgkmcnt(0)
	s_barrier
;     __device__ __forceinline__ void mainloop(bfr* smem, const AL& al, const BL& bl) {
;     ...
;         if constexpr (BL::DEPTH == 3) {
; #pragma unroll
;             for (int kt = 0; kt < nk; kt += 6) {
;                 G_STEP(0, fa0, fb0, fa1, fb1, 1, sa2, sb2, 2, 3);
;                 G_STEP(1, fa1, fb1, fa0, fb0, 2, sa0, sb0, 0, 3);
;                 G_STEP(2, fa0, fb0, fa1, fb1, 0, sa1, sb1, 1, 3);
;                 G_STEP(3, fa1, fb1, fa0, fb0, 1, sa2, sb2, 2, 3);
;                 G_STEP(4, fa0, fb0, fa1, fb1, 2, sa0, sb0, 0, 3);
;                 G_STEP(5, fa1, fb1, fa0, fb0, 0, sa1, sb1, 1, 3);
;             }
	v_mfma_f32_32x32x16_bf16 v[50:65], v[86:89], v[178:181], v[50:65]
	ds_read_b128 v[82:85], v132 offset:20496
	ds_read_b128 v[170:173], v133
	v_mfma_f32_32x32x16_bf16 v[34:49], v[86:89], v[182:185], v[34:49]
	ds_read_b128 v[86:89], v132 offset:23056
	ds_read_b128 v[174:177], v134
	v_mfma_f32_32x32x16_bf16 v[18:33], v[90:93], v[178:181], v[18:33]
	ds_read_b128 v[178:181], v132 offset:20528
	ds_read_b128 v[190:193], v135
	v_mfma_f32_32x32x16_bf16 v[2:17], v[90:93], v[182:185], v[2:17]
	ds_read_b128 v[90:93], v132 offset:23088
	ds_read_b128 v[182:185], v136
	v_mfma_f32_32x32x16_bf16 v[50:65], v[158:161], v[186:189], v[50:65]
	s_waitcnt vmcnt(8)
	ds_write_b128 v128, v[66:69] offset:40976
	s_waitcnt vmcnt(7)
	ds_write_b128 v129, v[70:73] offset:40976
	v_mfma_f32_32x32x16_bf16 v[34:49], v[158:161], v[166:169], v[34:49]
	s_waitcnt vmcnt(6)
	ds_write_b128 v137, v[74:77]
	v_mfma_f32_32x32x16_bf16 v[18:33], v[78:81], v[186:189], v[18:33]
	global_load_dwordx4 v[66:69], v[114:115], off offset:1856
	global_load_dwordx4 v[74:77], v[116:117], off offset:1856
	global_load_dwordx4 v[70:73], v[118:119], off offset:1856
	v_mfma_f32_32x32x16_bf16 v[2:17], v[78:81], v[166:169], v[2:17]
	s_waitcnt lgkmcnt(0)
	s_barrier
	v_mfma_f32_32x32x16_bf16 v[50:65], v[82:85], v[170:173], v[50:65]
	ds_read_b128 v[158:161], v132 offset:40976
	ds_read_b128 v[166:169], v138
	v_mfma_f32_32x32x16_bf16 v[34:49], v[82:85], v[174:177], v[34:49]
	ds_read_b128 v[186:189], v132 offset:43536
	ds_read_b128 v[194:197], v139
	v_mfma_f32_32x32x16_bf16 v[18:33], v[86:89], v[170:173], v[18:33]
	ds_read_b128 v[170:173], v132 offset:41008
	ds_read_b128 v[198:201], v140
	v_mfma_f32_32x32x16_bf16 v[2:17], v[86:89], v[174:177], v[2:17]
	ds_read_b128 v[174:177], v132 offset:43568
	ds_read_b128 v[204:207], v141
	v_mfma_f32_32x32x16_bf16 v[50:65], v[178:181], v[190:193], v[50:65]
	s_waitcnt vmcnt(8)
	ds_write_b128 v128, v[102:105] offset:16
	s_waitcnt vmcnt(7)
	ds_write_b128 v129, v[154:157] offset:16
	v_mfma_f32_32x32x16_bf16 v[34:49], v[178:181], v[182:185], v[34:49]
	s_waitcnt vmcnt(6)
	ds_write_b128 v128, v[162:165] offset:61456
	v_mfma_f32_32x32x16_bf16 v[18:33], v[90:93], v[190:193], v[18:33]
	global_load_dwordx4 v[86:89], v[114:115], off offset:1920
	global_load_dwordx4 v[78:81], v[116:117], off offset:1920
	global_load_dwordx4 v[82:85], v[118:119], off offset:1920
	v_mfma_f32_32x32x16_bf16 v[2:17], v[90:93], v[182:185], v[2:17]
	s_waitcnt lgkmcnt(0)
	s_barrier
	v_mfma_f32_32x32x16_bf16 v[50:65], v[158:161], v[166:169], v[50:65]
	ds_read_b128 v[102:105], v132 offset:16
	ds_read_b128 v[154:157], v142 offset:61456
	v_mfma_f32_32x32x16_bf16 v[34:49], v[158:161], v[194:197], v[34:49]
	ds_read_b128 v[158:161], v132 offset:2576
	ds_read_b128 v[162:165], v142 offset:64016
	v_mfma_f32_32x32x16_bf16 v[18:33], v[186:189], v[166:169], v[18:33]
	ds_read_b128 v[166:169], v132 offset:48
	ds_read_b128 v[178:181], v142 offset:61488
	v_mfma_f32_32x32x16_bf16 v[2:17], v[186:189], v[194:197], v[2:17]
	ds_read_b128 v[182:185], v132 offset:2608
	ds_read_b128 v[186:189], v143 offset:64016
	v_mfma_f32_32x32x16_bf16 v[50:65], v[170:173], v[198:201], v[50:65]
	s_waitcnt vmcnt(8)
	ds_write_b128 v128, v[94:97] offset:20496
	s_waitcnt vmcnt(7)
	ds_write_b128 v129, v[98:101] offset:20496
	v_mfma_f32_32x32x16_bf16 v[34:49], v[170:173], v[204:207], v[34:49]
	s_waitcnt vmcnt(6)
	ds_write_b128 v130, v[106:109]
	v_mfma_f32_32x32x16_bf16 v[18:33], v[174:177], v[198:201], v[18:33]
	global_load_dwordx4 v[98:101], v[114:115], off offset:1984
	global_load_dwordx4 v[90:93], v[116:117], off offset:1984
	global_load_dwordx4 v[94:97], v[118:119], off offset:1984
	v_mfma_f32_32x32x16_bf16 v[2:17], v[174:177], v[204:207], v[2:17]
	s_waitcnt lgkmcnt(0)
	s_barrier
	v_mfma_f32_32x32x16_bf16 v[50:65], v[102:105], v[154:157], v[50:65]
	ds_read_b128 v[106:109], v132 offset:20496
	ds_read_b128 v[170:173], v133
	v_mfma_f32_32x32x16_bf16 v[34:49], v[102:105], v[162:165], v[34:49]
	ds_read_b128 v[102:105], v132 offset:23056
	ds_read_b128 v[174:177], v134
	v_mfma_f32_32x32x16_bf16 v[18:33], v[158:161], v[154:157], v[18:33]
	ds_read_b128 v[154:157], v132 offset:20528
	ds_read_b128 v[190:193], v135
	v_mfma_f32_32x32x16_bf16 v[2:17], v[158:161], v[162:165], v[2:17]
	ds_read_b128 v[158:161], v132 offset:23088
	ds_read_b128 v[162:165], v136
	v_mfma_f32_32x32x16_bf16 v[50:65], v[166:169], v[178:181], v[50:65]
	s_waitcnt vmcnt(8)
	ds_write_b128 v128, v[66:69] offset:40976
	s_waitcnt vmcnt(7)
	ds_write_b128 v129, v[74:77] offset:40976
	v_mfma_f32_32x32x16_bf16 v[34:49], v[166:169], v[186:189], v[34:49]
	s_waitcnt vmcnt(6)
	ds_write_b128 v137, v[70:73]
	v_mfma_f32_32x32x16_bf16 v[18:33], v[182:185], v[178:181], v[18:33]
	v_mfma_f32_32x32x16_bf16 v[2:17], v[182:185], v[186:189], v[2:17]
	s_waitcnt lgkmcnt(0)
	s_barrier
;     __device__ __forceinline__ void mainloop(bfr* smem, const AL& al, const BL& bl) {
;     ...
;         if constexpr (BL::DEPTH == 3) {
; #pragma unroll
;             for (int kt = 0; kt < nk; kt += 6) {
;                 G_STEP(0, fa0, fb0, fa1, fb1, 1, sa2, sb2, 2, 3);
;                 G_STEP(1, fa1, fb1, fa0, fb0, 2, sa0, sb0, 0, 3);
;                 G_STEP(2, fa0, fb0, fa1, fb1, 0, sa1, sb1, 1, 3);
;                 G_STEP(3, fa1, fb1, fa0, fb0, 1, sa2, sb2, 2, 3);
;                 G_STEP(4, fa0, fb0, fa1, fb1, 2, sa0, sb0, 0, 3);
;                 G_STEP(5, fa1, fb1, fa0, fb0, 0, sa1, sb1, 1, 3);
;             }
; __device__ __forceinline__ void phase_inproj0(const Params& P, bfr* smem, int bid, int nb) {
;     ...
;         const int un = u + nb;
	v_mfma_f32_32x32x16_bf16 v[50:65], v[106:109], v[170:173], v[50:65]
	ds_read_b128 v[166:169], v132 offset:40976
	ds_read_b128 v[178:181], v138
	v_mfma_f32_32x32x16_bf16 v[34:49], v[106:109], v[174:177], v[34:49]
	ds_read_b128 v[106:109], v132 offset:43536
	ds_read_b128 v[182:185], v139
	v_mfma_f32_32x32x16_bf16 v[18:33], v[102:105], v[170:173], v[18:33]
	ds_read_b128 v[170:173], v132 offset:41008
	ds_read_b128 v[186:189], v140
	v_mfma_f32_32x32x16_bf16 v[2:17], v[102:105], v[174:177], v[2:17]
	ds_read_b128 v[102:105], v132 offset:43568
	ds_read_b128 v[174:177], v141
	v_mfma_f32_32x32x16_bf16 v[50:65], v[154:157], v[190:193], v[50:65]
	s_waitcnt vmcnt(5)
	ds_write_b128 v128, v[86:89] offset:16
	s_waitcnt vmcnt(4)
	ds_write_b128 v129, v[78:81] offset:16
	v_mfma_f32_32x32x16_bf16 v[34:49], v[154:157], v[162:165], v[34:49]
	s_waitcnt vmcnt(3)
	ds_write_b128 v128, v[82:85] offset:61456
	v_mfma_f32_32x32x16_bf16 v[18:33], v[158:161], v[190:193], v[18:33]
	v_mfma_f32_32x32x16_bf16 v[2:17], v[158:161], v[162:165], v[2:17]
	s_waitcnt lgkmcnt(0)
	s_barrier
	v_mfma_f32_32x32x16_bf16 v[50:65], v[166:169], v[178:181], v[50:65]
	ds_read_b128 v[154:157], v132 offset:16
	ds_read_b128 v[158:161], v142 offset:61456
	v_mfma_f32_32x32x16_bf16 v[34:49], v[166:169], v[182:185], v[34:49]
	ds_read_b128 v[162:165], v132 offset:2576
	ds_read_b128 v[166:169], v142 offset:64016
	v_mfma_f32_32x32x16_bf16 v[18:33], v[106:109], v[178:181], v[18:33]
	ds_read_b128 v[178:181], v132 offset:48
	ds_read_b128 v[190:193], v142 offset:61488
	v_mfma_f32_32x32x16_bf16 v[2:17], v[106:109], v[182:185], v[2:17]
	ds_read_b128 v[106:109], v132 offset:2608
	ds_read_b128 v[182:185], v143 offset:64016
	v_mfma_f32_32x32x16_bf16 v[50:65], v[170:173], v[186:189], v[50:65]
	s_waitcnt vmcnt(2)
	ds_write_b128 v128, v[98:101] offset:20496
	s_waitcnt vmcnt(1)
	ds_write_b128 v129, v[90:93] offset:20496
	v_mfma_f32_32x32x16_bf16 v[34:49], v[170:173], v[174:177], v[34:49]
	s_waitcnt vmcnt(0)
	ds_write_b128 v130, v[94:97]
	v_mfma_f32_32x32x16_bf16 v[18:33], v[102:105], v[186:189], v[18:33]
	v_mfma_f32_32x32x16_bf16 v[2:17], v[102:105], v[174:177], v[2:17]
	s_waitcnt lgkmcnt(0)
	s_barrier
	v_mfma_f32_32x32x16_bf16 v[50:65], v[154:157], v[158:161], v[50:65]
	ds_read_b128 v[102:105], v132 offset:20496
	ds_read_b128 v[170:173], v133
	v_mfma_f32_32x32x16_bf16 v[34:49], v[154:157], v[166:169], v[34:49]
	ds_read_b128 v[154:157], v132 offset:23056
	ds_read_b128 v[174:177], v134
	v_mfma_f32_32x32x16_bf16 v[18:33], v[162:165], v[158:161], v[18:33]
	ds_read_b128 v[158:161], v132 offset:20528
	ds_read_b128 v[186:189], v135
	v_mfma_f32_32x32x16_bf16 v[2:17], v[162:165], v[166:169], v[2:17]
	ds_read_b128 v[162:165], v132 offset:23088
	ds_read_b128 v[166:169], v136
	v_mfma_f32_32x32x16_bf16 v[50:65], v[178:181], v[190:193], v[50:65]
	v_mfma_f32_32x32x16_bf16 v[34:49], v[178:181], v[182:185], v[34:49]
	v_mfma_f32_32x32x16_bf16 v[18:33], v[106:109], v[190:193], v[18:33]
	v_mfma_f32_32x32x16_bf16 v[2:17], v[106:109], v[182:185], v[2:17]
	s_waitcnt lgkmcnt(0)
	s_barrier
	v_mfma_f32_32x32x16_bf16 v[50:65], v[102:105], v[170:173], v[50:65]
	v_mfma_f32_32x32x16_bf16 v[34:49], v[102:105], v[174:177], v[34:49]
	v_mfma_f32_32x32x16_bf16 v[18:33], v[154:157], v[170:173], v[18:33]
	v_mfma_f32_32x32x16_bf16 v[2:17], v[154:157], v[174:177], v[2:17]
	v_mfma_f32_32x32x16_bf16 v[50:65], v[158:161], v[186:189], v[50:65]
	v_mfma_f32_32x32x16_bf16 v[34:49], v[158:161], v[166:169], v[34:49]
	v_mfma_f32_32x32x16_bf16 v[18:33], v[162:165], v[186:189], v[18:33]
	v_mfma_f32_32x32x16_bf16 v[2:17], v[162:165], v[166:169], v[2:17]
	v_readlane_b32 s6, v253, 10
	s_add_i32 s19, s8, s6
	s_cmpk_lg_u32 s6, 0x100
	s_cbranch_scc1 .Lip2_u
	s_add_i32 s96, s96, 32
	s_mul_i32 s19, s96, 10923
	s_lshr_b32 s19, s19, 16
	s_mul_i32 s19, s19, 42
	s_add_i32 s19, s19, s96
	s_and_b32 s98, s44, 1
	s_mul_i32 s98, s98, 24
	s_add_i32 s19, s19, s98
	s_bfe_u32 s98, s44, 0x20001
	s_mul_i32 s98, s98, 6
	s_add_i32 s19, s19, s98
